# adds: the first workgroup of an XCD to arrive at a grid barrier starts an early L2 write-back
# speedup vs baseline: 1.0122x; 1.0007x over previous
.LBB0_148:
	s_lshl_b32 s0, s27, 8
	s_add_u32 s4, s16, s0
	s_addc_u32 s5, s17, 0
	v_mov_b32_e32 v2, 0x1000
	v_mov_b32_e32 v4, 1
	global_atomic_add v4, v2, v4, s[4:5] offset:1024 sc0
	buffer_inv sc1
	v_cvt_f32_u32_e32 v2, v3
	v_sub_u32_e32 v5, 0, v3
	v_rcp_iflag_f32_e32 v2, v2
	s_nop 0
	v_mul_f32_e32 v2, 0x4f7ffffe, v2
	v_cvt_u32_f32_e32 v2, v2
	v_mul_lo_u32 v5, v5, v2
	v_mul_hi_u32 v5, v2, v5
	v_add_u32_e32 v2, v2, v5
	s_waitcnt vmcnt(0)
	v_mul_hi_u32 v2, v4, v2
	v_mul_lo_u32 v5, v2, v3
	v_sub_u32_e32 v5, v4, v5
	v_add_u32_e32 v6, 1, v2
	v_cmp_ge_u32_e32 vcc, v5, v3
	v_add_u32_e32 v4, 1, v4
	s_nop 0
	v_cndmask_b32_e32 v2, v2, v6, vcc
	v_sub_u32_e32 v6, v5, v3
	v_cndmask_b32_e32 v5, v5, v6, vcc
	v_add_u32_e32 v6, 1, v2
	v_cmp_ge_u32_e32 vcc, v5, v3
	s_nop 1
	v_cndmask_b32_e32 v2, v2, v6, vcc
	v_mul_lo_u32 v5, v3, v2
	v_add_u32_e32 v3, v5, v3
	v_cmp_ne_u32_e32 vcc, v4, v3
	s_and_saveexec_b64 s[0:1], vcc
	s_xor_b64 s[0:1], exec, s[0:1]
	s_cbranch_execz .LBB0_162
	v_add_u32_e32 v6, 1, v5
	v_cmp_eq_u32_e32 vcc, v4, v6
	s_nop 4
	s_cbranch_vccz .Lhelp_skip_0
	buffer_wbl2 sc1
.Lhelp_skip_0:
	s_waitcnt lgkmcnt(0)
	v_mov_b32_e32 v1, 0x2000
	global_load_dword v1, v1, s[4:5] offset:1024 sc1
	s_add_u32 s10, s4, 0x2400
	s_addc_u32 s11, s5, 0
	s_waitcnt vmcnt(0)
	v_cmp_eq_u32_e32 vcc, v1, v2
	s_and_saveexec_b64 s[6:7], vcc
	s_cbranch_execz .LBB0_161
	v_readlane_b32 s8, v254, 2
	v_readlane_b32 s9, v254, 3
	s_add_u32 s8, s8, 0x4200
	s_addc_u32 s9, s9, 0
	s_mov_b32 s24, 1
	s_mov_b64 s[12:13], 0
	v_mov_b32_e32 v1, 0
	s_branch .LBB0_152

.LBB0_257:
	v_readlane_b32 s0, v254, 57
	v_readlane_b32 s1, v254, 58
	v_cvt_f32_u32_e32 v1, v3
	v_sub_u32_e32 v5, 0, v3
	v_rcp_iflag_f32_e32 v1, v1
	s_nop 1
	global_atomic_add v4, v34, v235, s[0:1] sc0
	buffer_inv sc1
	v_mul_f32_e32 v1, 0x4f7ffffe, v1
	v_cvt_u32_f32_e32 v1, v1
	v_mul_lo_u32 v5, v5, v1
	v_mul_hi_u32 v5, v1, v5
	v_add_u32_e32 v1, v1, v5
	s_waitcnt vmcnt(0)
	v_mul_hi_u32 v1, v4, v1
	v_mul_lo_u32 v5, v1, v3
	v_sub_u32_e32 v5, v4, v5
	v_add_u32_e32 v6, 1, v1
	v_cmp_ge_u32_e32 vcc, v5, v3
	v_add_u32_e32 v4, 1, v4
	s_nop 0
	v_cndmask_b32_e32 v1, v1, v6, vcc
	v_sub_u32_e32 v6, v5, v3
	v_cndmask_b32_e32 v5, v5, v6, vcc
	v_add_u32_e32 v6, 1, v1
	v_cmp_ge_u32_e32 vcc, v5, v3
	s_nop 1
	v_cndmask_b32_e32 v1, v1, v6, vcc
	v_mul_lo_u32 v5, v3, v1
	v_add_u32_e32 v3, v5, v3
	v_cmp_ne_u32_e32 vcc, v4, v3
	s_and_saveexec_b64 s[0:1], vcc
	s_xor_b64 s[0:1], exec, s[0:1]
	s_cbranch_execz .LBB0_271
	v_add_u32_e32 v6, 1, v5
	v_cmp_eq_u32_e32 vcc, v4, v6
	s_nop 4
	s_cbranch_vccz .Lhelp_skip_1
	buffer_wbl2 sc1
.Lhelp_skip_1:
	v_readlane_b32 s14, v254, 59
	v_readlane_b32 s15, v254, 60
	s_waitcnt lgkmcnt(0)
	s_nop 3
	global_load_dword v2, v34, s[14:15] sc1
	s_waitcnt vmcnt(0)
	v_cmp_eq_u32_e32 vcc, v2, v1
	s_and_saveexec_b64 s[14:15], vcc
	s_cbranch_execz .LBB0_270
	s_mov_b32 s40, 1
	s_mov_b64 s[16:17], 0
	s_branch .LBB0_261

.Lhelp_skip_3:
	v_readlane_b32 s14, v254, 59
	v_readlane_b32 s15, v254, 60
	s_waitcnt lgkmcnt(0)
	s_nop 3
	global_load_dword v2, v34, s[14:15] sc1
	s_waitcnt vmcnt(0)
	v_cmp_eq_u32_e32 vcc, v2, v1
	s_and_saveexec_b64 s[14:15], vcc
	s_cbranch_execz .LBB0_779
	s_mov_b32 s17, 1
	s_mov_b64 s[18:19], 0
	s_branch .LBB0_770

.Lhelp_skip_7:
	v_readlane_b32 s14, v254, 59
	v_readlane_b32 s15, v254, 60
	s_waitcnt lgkmcnt(0)
	s_nop 3
	global_load_dword v2, v34, s[14:15] sc1
	s_waitcnt vmcnt(0)
	v_cmp_eq_u32_e32 vcc, v2, v1
	s_and_saveexec_b64 s[14:15], vcc
	s_cbranch_execz .LBB0_1193
	s_mov_b32 s13, 1
	s_mov_b64 s[16:17], 0
	s_branch .LBB0_1184

.Lhelp_skip_8:
	v_readlane_b32 s14, v254, 59
	v_readlane_b32 s15, v254, 60
	s_waitcnt lgkmcnt(0)
	s_nop 3
	global_load_dword v2, v34, s[14:15] sc1
	s_waitcnt vmcnt(0)
	v_cmp_eq_u32_e32 vcc, v2, v1
	s_and_saveexec_b64 s[14:15], vcc
	s_cbranch_execz .LBB0_1286
	s_mov_b32 s20, 1
	s_mov_b64 s[16:17], 0
	s_branch .LBB0_1277
